# baseline (speedup 1.0000x reference)
_Z4k_l2PK15HIP_vector_typeIiLj4EES2_PKiPiS5_PKfPKDv8_DF16_S7_PDF16_SB_:
	s_mov_b64 s[88:89], s[0:1]
	s_mov_b32 s90, s2
	v_mov_b32_e32 v126, v0
.Ll2_reenter:
	s_mov_b64 s[4:5], -1
	s_cmpk_gt_u32 s2, 0x7c
	v_lshrrev_b32_e32 v64, 6, v0
	v_lshlrev_b32_e32 v1, 2, v0
	s_cbranch_scc0 .LBB2_34
	s_lshl_b32 s12, s2, 6
	v_or_b32_e32 v58, 0x200, v0
	s_load_dwordx4 s[4:7], s[0:1], 0x28
	s_load_dwordx2 s[8:9], s[0:1], 0x38
	s_addk_i32 s12, 0xe0c0
	v_lshrrev_b32_e32 v67, 5, v0
	v_lshrrev_b32_e32 v68, 5, v58
	v_or_b32_e32 v6, s12, v67
	v_or_b32_e32 v4, s12, v68
	v_and_b32_e32 v56, 0x7c, v1
	v_min_i32_e32 v2, 0xc34f, v6
	v_min_i32_e32 v4, 0xc34f, v4
	v_lshlrev_b32_e32 v18, 2, v56
	v_mov_b32_e32 v19, 0
	v_ashrrev_i32_e32 v3, 31, v2
	v_ashrrev_i32_e32 v5, 31, v4
	s_waitcnt lgkmcnt(0)
	v_lshl_add_u64 v[54:55], s[4:5], 0, v[18:19]
	v_lshlrev_b64 v[2:3], 9, v[2:3]
	v_lshlrev_b64 v[4:5], 9, v[4:5]
	v_lshl_add_u64 v[2:3], v[54:55], 0, v[2:3]
	v_lshl_add_u64 v[4:5], v[54:55], 0, v[4:5]
	global_load_dwordx4 v[26:29], v[2:3], off nt
	global_load_dwordx4 v[22:25], v[4:5], off nt
	v_or_b32_e32 v4, 0x600, v0
	v_or_b32_e32 v2, 32, v6
	v_lshrrev_b32_e32 v69, 5, v4
	v_min_i32_e32 v2, 0xc34f, v2
	v_or_b32_e32 v4, s12, v69
	v_ashrrev_i32_e32 v3, 31, v2
	v_min_i32_e32 v4, 0xc34f, v4
	v_lshlrev_b64 v[2:3], 9, v[2:3]
	v_ashrrev_i32_e32 v5, 31, v4
	v_lshl_add_u64 v[2:3], v[54:55], 0, v[2:3]
	v_lshlrev_b64 v[4:5], 9, v[4:5]
	v_lshl_add_u64 v[4:5], v[54:55], 0, v[4:5]
	global_load_dwordx4 v[34:37], v[2:3], off nt
	global_load_dwordx4 v[30:33], v[4:5], off nt
	v_mul_u32_u24_e32 v2, 0xc0, v64
	v_add_lshl_u32 v18, v2, v0, 4
	global_load_dwordx4 v[14:17], v18, s[6:7]
	global_load_dwordx4 v[10:13], v18, s[6:7] offset:1024
	global_load_dwordx4 v[6:9], v18, s[6:7] offset:2048
	global_load_dwordx4 v[2:5], v18, s[6:7] offset:3072
	v_and_b32_e32 v18, 0x1c0, v0
	v_lshl_add_u64 v[20:21], s[8:9], 0, v[18:19]
	v_and_b32_e32 v18, 48, v0
	v_lshl_add_u64 v[18:19], v[20:21], 0, v[18:19]
	global_load_dwordx4 v[18:21], v[18:19], off
	s_add_i32 s14, s2, 0x106
	s_cmpk_lt_i32 s2, 0x208
	s_cselect_b64 s[8:9], -1, 0
	s_cmpk_gt_i32 s2, 0x207
	s_cbranch_scc1 .LBB2_3
	s_lshl_b32 s3, s14, 6
	v_or_b32_e32 v50, s3, v67
	v_min_i32_e32 v38, 0xc34f, v50
	v_ashrrev_i32_e32 v39, 31, v38
	v_lshlrev_b64 v[38:39], 9, v[38:39]
	v_lshl_add_u64 v[42:43], v[54:55], 0, v[38:39]
	v_or_b32_e32 v38, s3, v68
	v_min_i32_e32 v38, 0xc34f, v38
	v_ashrrev_i32_e32 v39, 31, v38
	v_lshlrev_b64 v[38:39], 9, v[38:39]
	v_lshl_add_u64 v[44:45], v[54:55], 0, v[38:39]
	global_load_dwordx4 v[46:49], v[42:43], off nt
	global_load_dwordx4 v[38:41], v[44:45], off nt
	v_or_b32_e32 v42, 32, v50
	v_min_i32_e32 v42, 0xc34f, v42
	v_ashrrev_i32_e32 v43, 31, v42
	v_lshlrev_b64 v[42:43], 9, v[42:43]
	v_lshl_add_u64 v[60:61], v[54:55], 0, v[42:43]
	v_or_b32_e32 v42, s3, v69
	v_min_i32_e32 v42, 0xc34f, v42
	v_ashrrev_i32_e32 v43, 31, v42
	v_lshlrev_b64 v[42:43], 9, v[42:43]
	v_lshl_add_u64 v[62:63], v[54:55], 0, v[42:43]
	global_load_dwordx4 v[50:53], v[60:61], off nt
	global_load_dwordx4 v[42:45], v[62:63], off nt
.LBB2_3:
	s_load_dwordx2 s[4:5], s[0:1], 0x48
	v_lshlrev_b32_e32 v73, 1, v56
	s_movk_i32 s10, 0x110
	s_waitcnt vmcnt(8)
	v_cvt_pk_f16_f32 v57, v28, v29
	v_cvt_pk_f16_f32 v56, v26, v27
	v_mad_u32_u24 v59, v67, s10, v73
	s_add_i32 s3, s2, 0x289
	ds_write_b64 v59, v[56:57]
	s_waitcnt vmcnt(7)
	v_cvt_pk_f16_f32 v57, v24, v25
	v_cvt_pk_f16_f32 v56, v22, v23
	v_mad_u32_u24 v60, v68, s10, v73
	s_cmpk_lt_i32 s2, 0x7d
	ds_write_b64 v60, v[56:57]
	s_waitcnt vmcnt(6)
	v_cvt_pk_f16_f32 v57, v36, v37
	v_cvt_pk_f16_f32 v56, v34, v35
	s_cselect_b64 s[6:7], -1, 0
	s_cmpk_gt_i32 s2, 0x7c
	ds_write_b64 v59, v[56:57] offset:8704
	s_waitcnt vmcnt(5)
	v_cvt_pk_f16_f32 v57, v32, v33
	v_cvt_pk_f16_f32 v56, v30, v31
	v_mad_u32_u24 v59, v69, s10, v73
	ds_write_b64 v59, v[56:57]
	s_waitcnt lgkmcnt(0)
	s_barrier
	s_cbranch_scc1 .LBB2_5
	s_lshl_b32 s10, s3, 6
	v_or_b32_e32 v34, s10, v67
	v_min_i32_e32 v22, 0xc34f, v34
	v_ashrrev_i32_e32 v23, 31, v22
	v_lshlrev_b64 v[22:23], 9, v[22:23]
	v_lshl_add_u64 v[30:31], v[54:55], 0, v[22:23]
	v_or_b32_e32 v22, s10, v68
	v_min_i32_e32 v22, 0xc34f, v22
	v_ashrrev_i32_e32 v23, 31, v22
	v_lshlrev_b64 v[22:23], 9, v[22:23]
	v_lshl_add_u64 v[32:33], v[54:55], 0, v[22:23]
	global_load_dwordx4 v[26:29], v[30:31], off nt
	global_load_dwordx4 v[22:25], v[32:33], off nt
	v_or_b32_e32 v30, 32, v34
	v_min_i32_e32 v30, 0xc34f, v30
	v_ashrrev_i32_e32 v31, 31, v30
	v_lshlrev_b64 v[30:31], 9, v[30:31]
	v_lshl_add_u64 v[56:57], v[54:55], 0, v[30:31]
	v_or_b32_e32 v30, s10, v69
	v_min_i32_e32 v30, 0xc34f, v30
	v_ashrrev_i32_e32 v31, 31, v30
	v_lshlrev_b64 v[30:31], 9, v[30:31]
	v_lshl_add_u64 v[54:55], v[54:55], 0, v[30:31]
	global_load_dwordx4 v[34:37], v[56:57], off nt
	global_load_dwordx4 v[30:33], v[54:55], off nt

.LBB2_63:
	s_cmp_lt_u32 s90, 8
	s_cbranch_scc0 .Ll2_done
	s_mov_b64 exec, -1
	s_mov_b64 s[0:1], s[88:89]
	v_mov_b32_e32 v0, v126
	s_add_i32 s2, s90, 0x383
	s_mov_b32 s90, 0xffff
	s_branch .Ll2_reenter

	.amdhsa_kernel _Z4k_l2PK15HIP_vector_typeIiLj4EES2_PKiPiS5_PKfPKDv8_DF16_S7_PDF16_SB_
		.amdhsa_group_segment_fixed_size 53248
		.amdhsa_private_segment_fixed_size 0
		.amdhsa_kernarg_size 80
		.amdhsa_user_sgpr_count 2
		.amdhsa_user_sgpr_dispatch_ptr 0
		.amdhsa_user_sgpr_queue_ptr 0
		.amdhsa_user_sgpr_kernarg_segment_ptr 1
		.amdhsa_user_sgpr_dispatch_id 0
		.amdhsa_user_sgpr_kernarg_preload_length 0
		.amdhsa_user_sgpr_kernarg_preload_offset 0
		.amdhsa_user_sgpr_private_segment_size 0
		.amdhsa_uses_dynamic_stack 0
		.amdhsa_enable_private_segment 0
		.amdhsa_system_sgpr_workgroup_id_x 1
		.amdhsa_system_sgpr_workgroup_id_y 0
		.amdhsa_system_sgpr_workgroup_id_z 0
		.amdhsa_system_sgpr_workgroup_info 0
		.amdhsa_system_vgpr_workitem_id 0
		.amdhsa_next_free_vgpr 127
		.amdhsa_next_free_sgpr 91
		.amdhsa_accum_offset 128
		.amdhsa_reserve_vcc 1
		.amdhsa_float_round_mode_32 0
		.amdhsa_float_round_mode_16_64 0
		.amdhsa_float_denorm_mode_32 3
		.amdhsa_float_denorm_mode_16_64 3
		.amdhsa_dx10_clamp 1
		.amdhsa_ieee_mode 1
		.amdhsa_fp16_overflow 0
		.amdhsa_tg_split 0
		.amdhsa_exception_fp_ieee_invalid_op 0
		.amdhsa_exception_fp_denorm_src 0
		.amdhsa_exception_fp_ieee_div_zero 0
		.amdhsa_exception_fp_ieee_overflow 0
		.amdhsa_exception_fp_ieee_underflow 0
		.amdhsa_exception_fp_ieee_inexact 0
		.amdhsa_exception_int_div_zero 0
	.end_amdhsa_kernel

amdhsa.kernels:
  - .agpr_count:     0
    .args:
      - .actual_access:  read_only
        .address_space:  global
        .offset:         0
        .size:           8
        .value_kind:     global_buffer
      - .actual_access:  read_only
        .address_space:  global
        .offset:         8
        .size:           8
        .value_kind:     global_buffer
      - .actual_access:  read_only
        .address_space:  global
        .offset:         16
        .size:           8
        .value_kind:     global_buffer
      - .actual_access:  read_only
        .address_space:  global
        .offset:         24
        .size:           8
        .value_kind:     global_buffer
      - .address_space:  global
        .offset:         32
        .size:           8
        .value_kind:     global_buffer
      - .actual_access:  read_only
        .address_space:  global
        .offset:         40
        .size:           8
        .value_kind:     global_buffer
      - .actual_access:  read_only
        .address_space:  global
        .offset:         48
        .size:           8
        .value_kind:     global_buffer
      - .actual_access:  read_only
        .address_space:  global
        .offset:         56
        .size:           8
        .value_kind:     global_buffer
      - .actual_access:  read_only
        .address_space:  global
        .offset:         64
        .size:           8
        .value_kind:     global_buffer
      - .actual_access:  write_only
        .address_space:  global
        .offset:         72
        .size:           8
        .value_kind:     global_buffer
    .group_segment_fixed_size: 163796
    .kernarg_segment_align: 8
    .kernarg_segment_size: 80
    .language:       OpenCL C
    .language_version:
      - 2
      - 0
    .max_flat_workgroup_size: 1024
    .name:           _Z7k_attn3PKDF16_S0_PKiS2_PiPKDv8_DF16_PKfS6_S8_Pf
    .private_segment_fixed_size: 0
    .sgpr_count:     79
    .sgpr_spill_count: 0
    .symbol:         _Z7k_attn3PKDF16_S0_PKiS2_PiPKDv8_DF16_PKfS6_S8_Pf.kd
    .uniform_work_group_size: 1
    .uses_dynamic_stack: false
    .vgpr_count:     128
    .vgpr_spill_count: 0
    .wavefront_size: 64
  - .agpr_count:     0
    .args:
      - .actual_access:  read_only
        .address_space:  global
        .offset:         0
        .size:           8
        .value_kind:     global_buffer
      - .actual_access:  write_only
        .address_space:  global
        .offset:         8
        .size:           8
        .value_kind:     global_buffer
      - .actual_access:  read_only
        .address_space:  global
        .offset:         16
        .size:           8
        .value_kind:     global_buffer
      - .actual_access:  read_only
        .address_space:  global
        .offset:         24
        .size:           8
        .value_kind:     global_buffer
      - .actual_access:  read_only
        .address_space:  global
        .offset:         32
        .size:           8
        .value_kind:     global_buffer
      - .actual_access:  read_only
        .address_space:  global
        .offset:         40
        .size:           8
        .value_kind:     global_buffer
      - .actual_access:  read_only
        .address_space:  global
        .offset:         48
        .size:           8
        .value_kind:     global_buffer
      - .actual_access:  read_only
        .address_space:  global
        .offset:         56
        .size:           8
        .value_kind:     global_buffer
      - .actual_access:  read_only
        .address_space:  global
        .offset:         64
        .size:           8
        .value_kind:     global_buffer
      - .actual_access:  write_only
        .address_space:  global
        .offset:         72
        .size:           8
        .value_kind:     global_buffer
      - .actual_access:  write_only
        .address_space:  global
        .offset:         80
        .size:           8
        .value_kind:     global_buffer
      - .actual_access:  write_only
        .address_space:  global
        .offset:         88
        .size:           8
        .value_kind:     global_buffer
      - .actual_access:  write_only
        .address_space:  global
        .offset:         96
        .size:           8
        .value_kind:     global_buffer
    .group_segment_fixed_size: 1024
    .kernarg_segment_align: 8
    .kernarg_segment_size: 104
    .language:       OpenCL C
    .language_version:
      - 2
      - 0
    .max_flat_workgroup_size: 512
    .name:           _Z4k_l1PK15HIP_vector_typeIiLj4EEPiPKfS5_S5_S5_S5_S5_S5_PDF16_PfS6_S6_
    .private_segment_fixed_size: 0
    .sgpr_count:     22
    .sgpr_spill_count: 0
    .symbol:         _Z4k_l1PK15HIP_vector_typeIiLj4EEPiPKfS5_S5_S5_S5_S5_S5_PDF16_PfS6_S6_.kd
    .uniform_work_group_size: 1
    .uses_dynamic_stack: false
    .vgpr_count:     24
    .vgpr_spill_count: 0
    .wavefront_size: 64
  - .agpr_count:     0
    .args:
      - .actual_access:  read_only
        .address_space:  global
        .offset:         0
        .size:           8
        .value_kind:     global_buffer
      - .actual_access:  read_only
        .address_space:  global
        .offset:         8
        .size:           8
        .value_kind:     global_buffer
      - .actual_access:  read_only
        .address_space:  global
        .offset:         16
        .size:           8
        .value_kind:     global_buffer
      - .actual_access:  write_only
        .address_space:  global
        .offset:         24
        .size:           8
        .value_kind:     global_buffer
      - .actual_access:  write_only
        .address_space:  global
        .offset:         32
        .size:           8
        .value_kind:     global_buffer
      - .actual_access:  read_only
        .address_space:  global
        .offset:         40
        .size:           8
        .value_kind:     global_buffer
      - .actual_access:  read_only
        .address_space:  global
        .offset:         48
        .size:           8
        .value_kind:     global_buffer
      - .actual_access:  read_only
        .address_space:  global
        .offset:         56
        .size:           8
        .value_kind:     global_buffer
      - .actual_access:  write_only
        .address_space:  global
        .offset:         64
        .size:           8
        .value_kind:     global_buffer
      - .actual_access:  write_only
        .address_space:  global
        .offset:         72
        .size:           8
        .value_kind:     global_buffer
    .group_segment_fixed_size: 53248
    .kernarg_segment_align: 8
    .kernarg_segment_size: 80
    .language:       OpenCL C
    .language_version:
      - 2
      - 0
    .max_flat_workgroup_size: 512
    .name:           _Z4k_l2PK15HIP_vector_typeIiLj4EES2_PKiPiS5_PKfPKDv8_DF16_S7_PDF16_SB_
    .private_segment_fixed_size: 0
    .sgpr_count:     34
    .sgpr_spill_count: 0
    .symbol:         _Z4k_l2PK15HIP_vector_typeIiLj4EES2_PKiPiS5_PKfPKDv8_DF16_S7_PDF16_SB_.kd
    .uniform_work_group_size: 1
    .uses_dynamic_stack: false
    .vgpr_count:     127
    .vgpr_spill_count: 0
    .wavefront_size: 64
